# speedup vs baseline: 1.0159x; 1.0159x over previous
.LBB1_77:
	s_add_i32 s71, s40, 0
	global_load_dword v6, v[168:169], off sc1
	s_cmp_gt_u32 s25, 11
	s_cselect_b64 s[18:19], -1, 0
	s_cmp_lt_u32 s25, 12
	s_cselect_b64 s[36:37], -1, 0
	s_and_b64 s[16:17], s[18:19], exec
	s_cselect_b32 s42, 4, 0
	s_lshl_b32 s26, s42, 3
	s_load_dwordx2 s[16:17], s[0:1], s26 offset:0x18
	s_add_u32 s34, s0, s26
	s_addc_u32 s35, s1, 0
	s_and_b64 s[38:39], s[18:19], exec
	s_cselect_b32 s26, 0x1800, 0
	v_lshl_add_u64 v[250:251], v[176:177], 0, s[26:27]
	s_waitcnt lgkmcnt(0)
	global_load_dword v180, v110, s[16:17]
	global_load_dword v252, v110, s[16:17] offset:256
	global_load_dword v182, v[250:251], off
	global_load_dword v183, v[250:251], off offset:512
	global_load_dword v186, v[250:251], off offset:1024
	global_load_dword v253, v[250:251], off offset:1280
	global_load_dword v255, v[250:251], off offset:768
	global_load_dword v254, v[250:251], off offset:256
	s_nor_b64 s[38:39], s[18:19], s[4:5]
	v_mov_b32_e32 v185, 0
	v_mov_b32_e32 v184, 0
	v_mov_b32_e32 v181, 0
	s_and_saveexec_b64 s[16:17], s[38:39]
	s_cbranch_execz .LBB1_89
	s_mul_i32 s26, s25, 0x3200
	v_lshl_add_u64 v[250:251], v[170:171], 0, s[26:27]
	global_load_dword v181, v[250:251], off
	v_lshl_add_u32 v250, s25, 7, v189
	ds_read2_b32 v[184:185], v250 offset1:16
.LBB1_89:
	s_or_b64 exec, exec, s[16:17]
	s_add_i32 s41, s25, -12
	s_and_b64 s[16:17], s[18:19], exec
	s_cselect_b32 s26, s41, s25
	s_cmp_lg_u32 s26, 0
	s_cselect_b64 s[16:17], -1, 0
	s_cmp_eq_u32 s26, 0
	s_cselect_b64 s[38:39], -1, 0
	global_load_dword v7, v[168:169], off sc1
	v_add_u32_e32 v249, v61, v207
	ds_read_b128 v[64:67], v249
	ds_read_b128 v[68:71], v249 offset:64
	ds_read_b128 v[78:81], v249 offset:256
	ds_read_b128 v[82:85], v249 offset:320
	ds_read_b128 v[86:89], v249 offset:512
	ds_read_b128 v[90:93], v249 offset:576
	global_load_dword v8, v[168:169], off sc1
	s_waitcnt lgkmcnt(5)
	v_mfma_f32_16x16x32_f16 a[0:3], v[64:67], a[8:11], 0
	s_waitcnt lgkmcnt(4)
	v_mfma_f32_16x16x32_f16 a[0:3], v[68:71], a[12:15], a[0:3]
	s_waitcnt lgkmcnt(3)
	v_mfma_f32_16x16x32_f16 a[0:3], v[78:81], a[24:27], a[0:3]
	s_waitcnt lgkmcnt(2)
	v_mfma_f32_16x16x32_f16 a[0:3], v[82:85], a[28:31], a[0:3]
	s_waitcnt lgkmcnt(1)
	v_mfma_f32_16x16x32_f16 a[0:3], v[86:89], a[40:43], a[0:3]
	s_waitcnt lgkmcnt(0)
	v_mfma_f32_16x16x32_f16 a[4:7], v[90:93], a[44:47], a[0:3]
	v_mfma_f32_16x16x32_f16 a[0:3], v[64:67], a[16:19], 0
	v_mfma_f32_16x16x32_f16 a[0:3], v[68:71], a[20:23], a[0:3]
	v_mfma_f32_16x16x32_f16 a[0:3], v[78:81], a[32:35], a[0:3]
	v_mfma_f32_16x16x32_f16 a[0:3], v[82:85], a[36:39], a[0:3]
	v_mfma_f32_16x16x32_f16 a[0:3], v[86:89], a[48:51], a[0:3]
	v_mfma_f32_16x16x32_f16 a[0:3], v[90:93], a[52:55], a[0:3]
	global_load_dword v9, v[168:169], off sc1

.Lpl0_done:
.LBB1_87:
	s_cmp_lt_u32 s25, 12
	s_cbranch_scc0 .Lp0_pay
	s_waitcnt vmcnt(4) lgkmcnt(0)
	s_and_saveexec_b64 s[68:69], s[6:7]
	v_add_u32_e32 v0, 0x8400, v60
	ds_write2_b32 v0, v181, v184 offset1:16
	ds_write_b32 v60, v185 offset:33920
	s_mov_b64 exec, s[68:69]
	s_waitcnt lgkmcnt(0)
	s_barrier
	buffer_load_dwordx4 v[54:57], v194, s[20:23], 0 offen sc1
	buffer_load_dwordx4 v[50:53], v195, s[20:23], 0 offen sc1
	buffer_load_dwordx4 v[46:49], v196, s[20:23], 0 offen sc1
	buffer_load_dwordx4 v[42:45], v197, s[20:23], 0 offen sc1
	buffer_load_dwordx4 v[38:41], v198, s[20:23], 0 offen sc1
	buffer_load_dwordx4 v[34:37], v199, s[20:23], 0 offen sc1
	s_branch .LBB1_106

.Lp0_pay2:
	buffer_load_dwordx4 v[30:33], v200, s[20:23], 0 offen sc1
	buffer_load_dwordx4 v[26:29], v201, s[20:23], 0 offen sc1
	buffer_load_dwordx4 v[22:25], v202, s[20:23], 0 offen sc1
	buffer_load_dwordx4 v[18:21], v203, s[20:23], 0 offen sc1
	buffer_load_dwordx4 v[14:17], v204, s[20:23], 0 offen sc1
	buffer_load_dwordx4 v[10:13], v205, s[20:23], 0 offen sc1
	buffer_load_dwordx4 v[6:9], v206, s[20:23], 0 offen sc1
	ds_read_b128 v[64:67], v208 offset:34832
	ds_read_b128 v[68:71], v208 offset:48144
	ds_read_b128 v[78:81], v209 offset:34832
	ds_read_b128 v[82:85], v209 offset:48144
	ds_read_b128 v[86:89], v210 offset:34832
	ds_read_b128 v[90:93], v210 offset:48144
	ds_read_b128 v[94:97], v211 offset:34832
	ds_read_b128 v[98:101], v211 offset:48144
	ds_read_b128 v[190:193], v212 offset:34832
	ds_read_b128 v[102:105], v212 offset:48144
	ds_read_b128 v[106:109], v213 offset:34832
	ds_read_b128 v[114:117], v213 offset:48144
	ds_read_b128 v[118:121], v214 offset:34832
	ds_read_b128 v[122:125], v214 offset:48144
	ds_read_b128 v[126:129], v215 offset:34832
	ds_read_b128 v[130:133], v215 offset:48144
	ds_read_b128 v[134:137], v216 offset:34832
	ds_read_b128 v[138:141], v216 offset:48144
	ds_read_b128 v[142:145], v217 offset:34832
	ds_read_b128 v[146:149], v217 offset:48144
	ds_read_b128 v[150:153], v218 offset:34832
	ds_read_b128 v[154:157], v218 offset:48144
	ds_read_b128 v[158:161], v219 offset:34832
	ds_read_b128 v[162:165], v219 offset:48144
	ds_read_b128 v[72:75], v220 offset:34832
	ds_read_b128 v[0:3], v220 offset:48144
	s_andn2_b64 vcc, exec, s[36:37]
	s_mov_b64 s[36:37], -1
.Ltg0_entry:
	v_mov_b32_e32 v250, 0
	s_waitcnt vmcnt(12) lgkmcnt(14)
	v_or3_b32 v250, v250, v55, v57
	v_mfma_f32_16x16x32_f16 a[128:131], v[54:57], v[64:67], 0
	s_waitcnt vmcnt(11)
	v_or3_b32 v250, v250, v51, v53
	v_mfma_f32_16x16x32_f16 a[128:131], v[50:53], v[78:81], a[128:131]
	v_mfma_f32_16x16x32_f16 a[132:135], v[54:57], v[68:71], 0
	s_waitcnt vmcnt(10)
	v_or3_b32 v250, v250, v47, v49
	v_mfma_f32_16x16x32_f16 a[128:131], v[46:49], v[86:89], a[128:131]
	v_mfma_f32_16x16x32_f16 a[132:135], v[50:53], v[82:85], a[132:135]
	s_waitcnt vmcnt(9)
	v_or3_b32 v250, v250, v43, v45
	v_mfma_f32_16x16x32_f16 a[128:131], v[42:45], v[94:97], a[128:131]
	v_mfma_f32_16x16x32_f16 a[132:135], v[46:49], v[90:93], a[132:135]
	s_waitcnt vmcnt(8)
	v_or3_b32 v250, v250, v39, v41
	v_mfma_f32_16x16x32_f16 a[128:131], v[38:41], v[190:193], a[128:131]
	v_mfma_f32_16x16x32_f16 a[132:135], v[42:45], v[98:101], a[132:135]
	s_waitcnt vmcnt(7)
	v_or3_b32 v250, v250, v35, v37
	v_mfma_f32_16x16x32_f16 a[128:131], v[34:37], v[106:109], a[128:131]
	v_mfma_f32_16x16x32_f16 a[132:135], v[38:41], v[102:105], a[132:135]
	s_waitcnt vmcnt(6) lgkmcnt(13)
	v_or3_b32 v250, v250, v31, v33
	v_mfma_f32_16x16x32_f16 a[128:131], v[30:33], v[118:121], a[128:131]
	v_mfma_f32_16x16x32_f16 a[132:135], v[34:37], v[114:117], a[132:135]
	s_waitcnt vmcnt(5) lgkmcnt(11)
	v_or3_b32 v250, v250, v27, v29
	v_mfma_f32_16x16x32_f16 a[128:131], v[26:29], v[126:129], a[128:131]
	v_mfma_f32_16x16x32_f16 a[132:135], v[30:33], v[122:125], a[132:135]
	s_waitcnt vmcnt(4) lgkmcnt(9)
	v_or3_b32 v250, v250, v23, v25
	v_mfma_f32_16x16x32_f16 a[128:131], v[22:25], v[134:137], a[128:131]
	v_mfma_f32_16x16x32_f16 a[132:135], v[26:29], v[130:133], a[132:135]
	s_waitcnt vmcnt(3) lgkmcnt(7)
	v_or3_b32 v250, v250, v19, v21
	v_mfma_f32_16x16x32_f16 a[128:131], v[18:21], v[142:145], a[128:131]
	v_mfma_f32_16x16x32_f16 a[132:135], v[22:25], v[138:141], a[132:135]
	s_waitcnt vmcnt(2) lgkmcnt(5)
	v_or3_b32 v250, v250, v15, v17
	v_mfma_f32_16x16x32_f16 a[128:131], v[14:17], v[150:153], a[128:131]
	v_mfma_f32_16x16x32_f16 a[132:135], v[18:21], v[146:149], a[132:135]
	s_waitcnt vmcnt(1) lgkmcnt(3)
	v_or3_b32 v250, v250, v11, v13
	v_mfma_f32_16x16x32_f16 a[128:131], v[10:13], v[158:161], a[128:131]
	v_mfma_f32_16x16x32_f16 a[132:135], v[14:17], v[154:157], a[132:135]
	s_waitcnt vmcnt(0) lgkmcnt(0)
	v_or3_b32 v250, v250, v7, v9
	v_mfma_f32_16x16x32_f16 a[128:131], v[6:9], v[72:75], a[128:131]
	v_mfma_f32_16x16x32_f16 a[132:135], v[10:13], v[162:165], a[132:135]
	v_mfma_f32_16x16x32_f16 a[132:135], v[6:9], v[0:3], a[132:135]
	v_and_b32_e32 v250, s64, v250
	v_cmp_ne_u32_e64 s[66:67], 0, v250
	s_cmp_lg_u64 s[66:67], 0
	s_cbranch_scc1 .Ltg0_redo
.Ltg0_go:
	s_cmp_lt_u32 s25, 12
	s_cbranch_scc0 .Lfl0_skip
	s_or_b32 s70, s40, 1
	s_and_saveexec_b64 s[68:69], s[12:13]
	v_mov_b32_e32 v250, s70
	s_cmp_lg_u64 s[28:29], 0
	s_cbranch_scc0 .Lfl0_nf
	global_store_dword v[174:175], v250, off
	s_branch .Lfl0_done
.Lfl0_nf:
	global_store_dword v[174:175], v250, off sc1
.Lfl0_done:
	s_mov_b64 exec, s[68:69]
.Lfl0_skip:
	v_add_u32_e32 v250, v110, v226
	s_nop 1
	v_accvgpr_read_b32 v10, a128
	v_accvgpr_read_b32 v11, a129
	v_accvgpr_read_b32 v12, a130
	v_accvgpr_read_b32 v13, a131
	v_cvt_pk_f16_f32 v1, v12, v13
	v_cvt_pk_f16_f32 v0, v10, v11
	v_accvgpr_read_b32 v6, a132
	v_accvgpr_read_b32 v7, a133
	v_accvgpr_read_b32 v8, a134
	v_accvgpr_read_b32 v9, a135
	v_cvt_pk_f16_f32 v3, v8, v9
	v_cvt_pk_f16_f32 v2, v6, v7
	ds_write2_b64 v221, v[0:1], v[2:3] offset0:48 offset1:80
	s_cmp_lt_u32 s25, 12
	s_cbranch_scc0 .Lmd_dec
	s_waitcnt lgkmcnt(0)
	s_barrier
	s_branch .Lst1_entry
.LBB1_106:
	v_add_u32_e32 v184, v110, v224
	ds_read_b128 v[28:31], v225 offset:33792
	ds_read_b128 v[10:13], v225 offset:33856
	v_add_u32_e32 v250, v110, v226
	v_add_u32_e32 v185, v110, v227
	ds_read_b32 v20, v184 offset:21504
	ds_read_b32 v21, v250 offset:21504
	ds_read_b32 v22, v185 offset:21504
	ds_read_b128 v[14:17], v225 offset:33920
	v_add_u32_e32 v251, v110, v228
	ds_read_b32 v23, v251 offset:21504
	s_waitcnt lgkmcnt(6)
	v_mov_b32_e32 v0, v28
	s_waitcnt lgkmcnt(5)
	v_mov_b32_e32 v1, v10
	s_waitcnt vmcnt(10)
	v_mul_f32_e32 v2, v182, v28
	s_waitcnt vmcnt(10)
	v_pk_fma_f32 v[0:1], v[182:183], v[0:1], v[2:3] op_sel_hi:[1,1,0]
	s_waitcnt vmcnt(10) lgkmcnt(1)
	v_mul_f32_e32 v181, v186, v14
	v_accvgpr_read_b32 v0, a4
	v_pk_add_f32 v[0:1], v[180:181], v[0:1]
	v_mul_f32_e32 v2, v182, v29
	v_add_f32_e32 v0, v0, v1
	v_mul_f32_e32 v0, 0xbfb8aa3b, v0
	v_exp_f32_e32 v3, v0
	v_mov_b32_e32 v0, v29
	v_mov_b32_e32 v1, v11
	v_mul_f32_e32 v181, v186, v15
	v_pk_fma_f32 v[0:1], v[182:183], v[0:1], v[2:3] op_sel_hi:[1,1,0]
	v_mul_f32_e32 v2, v182, v30
	v_accvgpr_read_b32 v0, a5
	v_pk_add_f32 v[0:1], v[180:181], v[0:1]
	v_mul_f32_e32 v181, v186, v16
	v_add_f32_e32 v0, v0, v1
	v_mul_f32_e32 v0, 0xbfb8aa3b, v0
	v_exp_f32_e32 v0, v0
	v_add_f32_e32 v1, 1.0, v3
	v_rcp_f32_e32 v24, v1
	v_mov_b32_e32 v1, v12
	v_add_f32_e32 v3, 1.0, v0
	v_mov_b32_e32 v0, v30
	v_pk_fma_f32 v[0:1], v[182:183], v[0:1], v[2:3] op_sel_hi:[1,1,0]
	v_mul_f32_e32 v2, v182, v31
	v_accvgpr_read_b32 v0, a6
	v_pk_add_f32 v[0:1], v[180:181], v[0:1]
	v_mul_f32_e32 v181, v186, v17
	v_add_f32_e32 v0, v0, v1
	v_mul_f32_e32 v0, 0xbfb8aa3b, v0
	v_exp_f32_e32 v18, v0
	v_mov_b32_e32 v0, v31
	v_mov_b32_e32 v1, v13
	v_pk_fma_f32 v[0:1], v[182:183], v[0:1], v[2:3] op_sel_hi:[1,1,0]
	v_rcp_f32_e32 v25, v3
	v_accvgpr_read_b32 v0, a7
	v_pk_add_f32 v[0:1], v[180:181], v[0:1]
	s_andn2_b64 vcc, exec, s[28:29]
	s_mov_b64 s[16:17], vcc
	v_add_f32_e32 v0, v0, v1
	v_mul_f32_e32 v0, 0xbfb8aa3b, v0
	v_exp_f32_e32 v0, v0
	v_add_f32_e32 v1, 1.0, v18
	v_rcp_f32_e32 v26, v1
	v_mul_f32_e32 v1, v21, v25
	v_add_f32_e32 v0, 1.0, v0
	v_rcp_f32_e32 v27, v0
	v_mul_f32_e32 v2, v22, v26
	v_mul_f32_e32 v0, v20, v24
	v_cvt_pk_f16_f32 v18, v0, v1
	s_waitcnt lgkmcnt(0)
	v_mul_f32_e32 v3, v23, v27
	v_cvt_pk_f16_f32 v19, v2, v3
	v_or_b32_e32 v19, s64, v19
	s_cbranch_vccnz .LBB1_171
	global_store_dwordx2 v[172:173], v[18:19], off
	s_or_b32 s70, s40, 1
	s_cmp_lt_u32 s25, 12
	s_cbranch_scc1 .Lfl0_e1
	s_and_saveexec_b64 s[68:69], s[12:13]
	v_mov_b32_e32 v3, s70
	global_store_dword v[174:175], v3, off
	s_mov_b64 exec, s[68:69]
.Lfl0_e1:
	s_cbranch_execnz .LBB1_109
.LBB1_108:
	global_store_dwordx2 v[172:173], v[18:19], off sc1
	s_or_b32 s70, s40, 1
	s_cmp_lt_u32 s25, 12
	s_cbranch_scc1 .Lfl0_e2
	s_and_saveexec_b64 s[68:69], s[12:13]
	v_mov_b32_e32 v3, s70
	global_store_dword v[174:175], v3, off sc1
	s_mov_b64 exec, s[68:69]
.Lfl0_e2:
.LBB1_109:
	v_accvgpr_read_b32 v0, a0
	v_accvgpr_read_b32 v1, a1
	v_accvgpr_read_b32 v2, a2
	v_accvgpr_read_b32 v3, a3
	v_fma_mixlo_f16 v18, v20, v24, 0
	v_fma_mixlo_f16 v19, v21, v25, 0
	v_fma_mixlo_f16 v20, v22, v26, 0
	v_fma_mixlo_f16 v21, v23, v27, 0
	v_mul_f32_e32 v10, v255, v10
	v_fmac_f32_e32 v10, v254, v28
	v_add_f32_e32 v0, v252, v0
	v_fmac_f32_e32 v10, v253, v14
	v_add_f32_e32 v0, v0, v10
	v_mul_f32_e32 v0, 0xbfb8aa3b, v0
	v_exp_f32_e32 v0, v0
	v_mul_f32_e32 v28, v255, v11
	v_fmac_f32_e32 v28, v254, v29
	v_add_f32_e32 v1, v252, v1
	v_fmac_f32_e32 v28, v253, v15
	v_add_f32_e32 v1, v1, v28
	v_add_f32_e32 v0, 1.0, v0
	v_mul_f32_e32 v1, 0xbfb8aa3b, v1
	v_rcp_f32_e32 v0, v0
	v_exp_f32_e32 v1, v1
	ds_write_b32 v184, v0 offset:29696
	ds_write_b16 v247, v18 offset:12800
	v_add_f32_e32 v0, 1.0, v1
	v_add_f32_e32 v1, v252, v2
	v_mul_f32_e32 v2, v255, v12
	v_fmac_f32_e32 v2, v254, v30
	v_fmac_f32_e32 v2, v253, v16
	v_add_f32_e32 v1, v1, v2
	v_add_f32_e32 v2, v252, v3
	v_mul_f32_e32 v3, v255, v13
	v_fmac_f32_e32 v3, v254, v31
	v_mul_f32_e32 v1, 0xbfb8aa3b, v1
	v_fmac_f32_e32 v3, v253, v17
	v_rcp_f32_e32 v0, v0
	v_exp_f32_e32 v1, v1
	v_add_f32_e32 v2, v2, v3
	v_mul_f32_e32 v2, 0xbfb8aa3b, v2
	v_exp_f32_e32 v2, v2
	ds_write_b32 v250, v0 offset:29696
	v_add_f32_e32 v0, 1.0, v1
	v_rcp_f32_e32 v0, v0
	v_add_f32_e32 v1, 1.0, v2
	v_rcp_f32_e32 v1, v1
	ds_write_b16 v247, v19 offset:13344
	ds_write_b32 v185, v0 offset:29696
	ds_write_b16 v247, v20 offset:13888
	ds_write_b32 v251, v1 offset:29696
	ds_write_b16 v247, v21 offset:14432
	s_cmp_lt_u32 s25, 12
	s_cbranch_scc1 .Lp0_pay2
.Lst1_entry:
	s_xor_b64 s[30:31], s[30:31], -1
	s_andn2_b64 vcc, exec, s[30:31]
	s_mov_b64 s[30:31], -1
	s_add_i32 s71, s40, 1
	global_load_dword v50, v[168:169], off sc1
	global_load_dword v51, v[168:169], off sc1
	ds_read_b128 v[54:57], v208 offset:34832
	ds_read_b128 v[64:67], v208 offset:48144
	ds_read_b128 v[68:71], v209 offset:34832
	ds_read_b128 v[72:75], v209 offset:48144
	ds_read_b128 v[78:81], v210 offset:34832
	ds_read_b128 v[82:85], v210 offset:48144
	ds_read_b128 v[86:89], v211 offset:34832
	ds_read_b128 v[90:93], v211 offset:48144
	ds_read_b128 v[94:97], v212 offset:34832
	ds_read_b128 v[98:101], v212 offset:48144
	ds_read_b128 v[102:105], v213 offset:34832
	ds_read_b128 v[106:109], v213 offset:48144
	ds_read_b128 v[114:117], v214 offset:34832
	global_load_dword v52, v[168:169], off sc1
	ds_read_b128 v[118:121], v214 offset:48144
	ds_read_b128 v[122:125], v215 offset:34832
	ds_read_b128 v[126:129], v215 offset:48144
	ds_read_b128 v[130:133], v216 offset:34832
	ds_read_b128 v[134:137], v216 offset:48144
	ds_read_b128 v[138:141], v217 offset:34832
	ds_read_b128 v[142:145], v217 offset:48144
	ds_read_b128 v[146:149], v218 offset:34832
	ds_read_b128 v[150:153], v218 offset:48144
	ds_read_b128 v[154:157], v219 offset:34832
	ds_read_b128 v[158:161], v219 offset:48144
	ds_read_b128 v[162:165], v220 offset:34832
	ds_read_b128 v[180:183], v220 offset:48144
	global_load_dword v53, v[168:169], off sc1
